# E phase: per-column constant loads of a segment's first row issued before the wait on the first rows (one round trip instead of two)
# baseline (speedup 1.0000x reference)
; __device__ void phase_E_rows(const Params& p, int l, char* smem, int vb, int nvb, bool split, int nrows, int oz) {
;     ...
;         const int mr = isctx ? 8 : row / T;
;         if (mr != cur_mr) {
;             cur_mr = mr;
; #pragma unroll
;             for (int k = 0; k < 4; ++k) {
;                 const int col = (k >> 1) * 512 + lane * 8 + (k & 1) * 4;
;                 if (l > 0) {
;                     const float4 g = *(const float4*)(mod + ((l - 1) * 9 + mr) * 3072 + 2048 + col);
;                     const float4 pg = *(const float4*)(p.in[I_POSTG] + (l - 1) * DM + col);
;                     gp[k] = make_float4(g.x * pg.x, g.y * pg.y, g.z * pg.z, g.w * pg.w);
.LBB0_913:
	s_ashr_i32 s96, s56, 31
	s_lshr_b32 s96, s96, 21
	s_add_i32 s96, s56, s96
	s_ashr_i32 s96, s96, 11
	s_cmpk_gt_i32 s56, 0x3fff
	s_cselect_b32 s66, 8, s96
	s_add_i32 s28, s66, s48
	s_mulk_i32 s28, 0xc00
	s_ashr_i32 s29, s28, 31
	s_lshl_b64 s[28:29], s[28:29], 2
	s_add_u32 s28, s60, s28
	s_addc_u32 s29, s61, s29
	s_add_u32 s84, s28, 0x2000
	s_addc_u32 s85, s29, 0
	s_add_i32 s28, s66, s49
	s_mulk_i32 s28, 0xc00
	s_ashr_i32 s29, s28, 31
	s_lshl_b64 s[28:29], s[28:29], 2
	s_add_u32 s28, s60, s28
	s_addc_u32 s29, s61, s29
	s_add_u32 s82, s28, 0x1000
	s_addc_u32 s83, s29, 0
	v_lshlrev_b32_e32 v242, 2, v106
	v_lshlrev_b32_e32 v243, 2, v108
	v_lshlrev_b32_e32 v244, 2, v110
	s_and_b64 vcc, exec, s[44:45]
	s_cbranch_vccnz .Le_modE_noA
	global_load_dwordx4 v[118:121], v2, s[84:85]
	global_load_dwordx4 v[202:205], v[112:113], off
	global_load_dwordx4 v[122:125], v242, s[84:85]
	global_load_dwordx4 v[206:209], v[112:113], off offset:16
	global_load_dwordx4 v[126:129], v243, s[84:85]
	global_load_dwordx4 v[210:213], v[112:113], off offset:2048
	global_load_dwordx4 v[134:137], v244, s[84:85]
	global_load_dwordx4 v[214:217], v[112:113], off offset:2064

; __device__ void phase_E_rows(const Params& p, int l, char* smem, int vb, int nvb, bool split, int nrows, int oz) {
;     ...
;     E2_LOAD(nx0, nxb0, ny0, rbeg)
;     if (rbeg + 1 < rend) E2_LOAD(nx1, nxb1, ny1, rbeg + 1)
;     for (int row = rbeg; row < rend; ++row) {
;         const bool isctx = row >= LAT;
;         const int mr = isctx ? 8 : row / T;
;         if (mr != cur_mr) {
;             cur_mr = mr;
; #pragma unroll
;             for (int k = 0; k < 4; ++k) {
;                 const int col = (k >> 1) * 512 + lane * 8 + (k & 1) * 4;
;                 if (l > 0) {
;                     const float4 g = *(const float4*)(mod + ((l - 1) * 9 + mr) * 3072 + 2048 + col);
;                     const float4 pg = *(const float4*)(p.in[I_POSTG] + (l - 1) * DM + col);
;                     gp[k] = make_float4(g.x * pg.x, g.y * pg.y, g.z * pg.z, g.w * pg.w);
;                 }
;                 if (l < 4) {
;                     const float4 pre = *(const float4*)(p.in[I_PREG] + l * DM + col);
;                     const float4 sc = *(const float4*)(mod + (l * 9 + mr) * 3072 + 1024 + col);
;                     sh[k] = *(const float4*)(mod + (l * 9 + mr) * 3072 + col);
;                     pa[k] = make_float4(pre.x * (1.f + sc.x), pre.y * (1.f + sc.y), pre.z * (1.f + sc.z), pre.w * (1.f + sc.w));
;                 }
.Le_modE_noB:
	v_mov_b32_e32 v235, 1
	s_waitcnt vmcnt(0)
	v_mov_b64_e32 v[86:87], v[82:83]
	s_add_u32 s64, s78, s20
	v_mov_b64_e32 v[90:91], v[74:75]
	v_mov_b64_e32 v[94:95], v[78:79]
	v_mov_b64_e32 v[98:99], v[70:71]
	v_mov_b64_e32 v[84:85], v[80:81]
	s_addc_u32 s65, s79, s21
	s_mov_b32 s28, -1
	v_mov_b64_e32 v[88:89], v[72:73]
	v_mov_b64_e32 v[92:93], v[76:77]
	v_mov_b64_e32 v[96:97], v[68:69]
	v_mov_b64_e32 v[150:151], v[64:65]
	v_mov_b64_e32 v[152:153], v[66:67]
	v_mov_b64_e32 v[154:155], v[60:61]
	v_mov_b64_e32 v[156:157], v[62:63]
	v_mov_b64_e32 v[158:159], v[56:57]
	v_mov_b64_e32 v[160:161], v[58:59]
	v_mov_b64_e32 v[162:163], v[52:53]
	v_mov_b64_e32 v[164:165], v[54:55]
	v_mov_b32_e32 v234, 0
.LBB0_914:
	s_ashr_i32 s20, s56, 31
	s_lshr_b32 s20, s20, 21
	s_add_i32 s20, s56, s20
	s_ashr_i32 s29, s20, 11
	s_cmpk_gt_i32 s56, 0x3fff
	s_cselect_b64 s[20:21], -1, 0
	s_and_b64 s[46:47], s[20:21], exec
	s_cselect_b32 s66, 8, s29
	s_cmp_eq_u32 s66, s28
	s_cbranch_scc1 .LBB0_931
	s_add_i32 s28, s66, s48
	s_mulk_i32 s28, 0xc00
	s_ashr_i32 s29, s28, 31
	s_lshl_b64 s[28:29], s[28:29], 2
	s_add_u32 s28, s60, s28
	s_addc_u32 s29, s61, s29
	s_add_u32 s84, s28, 0x2000
	s_addc_u32 s85, s29, 0
	s_add_i32 s28, s66, s49
	s_mulk_i32 s28, 0xc00
	s_ashr_i32 s29, s28, 31
	s_lshl_b64 s[28:29], s[28:29], 2
	s_add_u32 s28, s60, s28
	s_addc_u32 s29, s61, s29
	s_add_u32 s82, s28, 0x1000
	v_cndmask_b32_e64 v245, 0, 1, s[50:51]
	s_addc_u32 s83, s29, 0
	v_cmp_ne_u32_e64 s[46:47], 1, v245
	v_lshlrev_b32_e32 v242, 2, v106
	v_lshlrev_b32_e32 v243, 2, v108
	v_lshlrev_b32_e32 v244, 2, v110
	v_readfirstlane_b32 s96, v235
	v_mov_b32_e32 v235, 0
	s_cmp_eq_u32 s96, 1
	s_cbranch_scc1 .Le_mod_noB
	s_and_b64 vcc, exec, s[44:45]
	s_cbranch_vccnz .Le_mod_noA
	global_load_dwordx4 v[118:121], v2, s[84:85]
	global_load_dwordx4 v[202:205], v[112:113], off
	global_load_dwordx4 v[122:125], v242, s[84:85]
	global_load_dwordx4 v[206:209], v[112:113], off offset:16
	global_load_dwordx4 v[126:129], v243, s[84:85]
	global_load_dwordx4 v[210:213], v[112:113], off offset:2048
	global_load_dwordx4 v[134:137], v244, s[84:85]
	global_load_dwordx4 v[214:217], v[112:113], off offset:2064
